# E26: E25 + the same back-edge rotation applied to the NSA sel-general and win-general tile loops
# baseline (speedup 1.0000x reference)
.LBB0_700:
	s_lshl_b32 s8, s36, 19
	s_cmp_gt_i32 s82, s86
	s_cbranch_scc1 .LBB0_781
	s_sub_i32 s36, s2, s43
	s_sub_i32 s84, 0, s42
	s_cmp_ge_i32 s82, s42
	s_mov_b64 s[0:1], -1
	s_cbranch_scc0 .LBB0_704
	s_branch .LBB0_703
	s_nop 0
	s_nop 0
	s_nop 0
	s_nop 0
	s_nop 0
	s_nop 0
	s_nop 0
	s_nop 0
	s_nop 0
	s_nop 0
	s_nop 0
	s_nop 0
	s_nop 0
	s_nop 0
	s_nop 0
	s_nop 0
	s_nop 0
	s_nop 0
	s_nop 0
	s_nop 0
	s_nop 0
	s_nop 0
	s_nop 0
	s_nop 0
	s_nop 0
	s_nop 0
	s_nop 0
	s_nop 0
	s_nop 0
	s_nop 0
	s_nop 0
	s_nop 0
	s_nop 0
	s_nop 0
.LBB0_703:
	s_add_i32 s0, s84, s82
	s_cmp_ge_i32 s0, s43
	s_cselect_b32 s1, s36, 0
	s_add_i32 s22, s0, s1
	s_mov_b64 s[0:1], 0

.Lx702_body:
	s_waitcnt lgkmcnt(0)
	v_mfma_f32_16x16x32_bf16 v[90:93], v[70:73], v[78:81], 0
	v_mfma_f32_16x16x32_bf16 v[70:73], v[70:73], v[82:85], 0
	v_add_u32_e32 v0, s0, v143
	ds_read_b128 v[198:201], v0
	ds_read_b128 v[202:205], v197 offset:1024
	ds_read_b128 v[206:209], v197 offset:5120
	v_mfma_f32_16x16x32_bf16 v[98:101], v[74:77], v[78:81], 0
	v_mfma_f32_16x16x32_bf16 v[74:77], v[74:77], v[82:85], 0
	v_mfma_f32_16x16x32_bf16 v[210:213], v[86:89], v[78:81], 0
	ds_read_b128 v[214:217], v0 offset:4096
	v_mfma_f32_16x16x32_bf16 v[86:89], v[86:89], v[82:85], 0
	v_mfma_f32_16x16x32_bf16 v[78:81], v[94:97], v[78:81], 0
	v_mfma_f32_16x16x32_bf16 v[82:85], v[94:97], v[82:85], 0
	ds_read_b128 v[94:97], v0 offset:8192
	s_waitcnt lgkmcnt(3)
	v_mfma_f32_16x16x32_bf16 v[90:93], v[198:201], v[202:205], v[90:93]
	s_waitcnt lgkmcnt(2)
	v_mfma_f32_16x16x32_bf16 v[70:73], v[198:201], v[206:209], v[70:73]
	ds_read_b128 v[198:201], v0 offset:12288
	v_add_u32_e32 v0, s0, v144
	s_waitcnt lgkmcnt(2)
	v_mfma_f32_16x16x32_bf16 v[98:101], v[214:217], v[202:205], v[98:101]
	v_mfma_f32_16x16x32_bf16 v[74:77], v[214:217], v[206:209], v[74:77]
	ds_read_b128 v[214:217], v0
	ds_read_b128 v[218:221], v197 offset:2048
	ds_read_b128 v[222:225], v197 offset:6144
	s_waitcnt lgkmcnt(4)
	v_mfma_f32_16x16x32_bf16 v[210:213], v[94:97], v[202:205], v[210:213]
	v_mfma_f32_16x16x32_bf16 v[86:89], v[94:97], v[206:209], v[86:89]
	ds_read_b128 v[94:97], v0 offset:4096
	s_waitcnt lgkmcnt(4)
	v_mfma_f32_16x16x32_bf16 v[78:81], v[198:201], v[202:205], v[78:81]
	ds_read_b128 v[202:205], v0 offset:8192
	v_mfma_f32_16x16x32_bf16 v[82:85], v[198:201], v[206:209], v[82:85]
	s_waitcnt lgkmcnt(3)
	v_mfma_f32_16x16x32_bf16 v[90:93], v[214:217], v[218:221], v[90:93]
	ds_read_b128 v[198:201], v0 offset:12288
	s_waitcnt lgkmcnt(3)
	v_mfma_f32_16x16x32_bf16 v[70:73], v[214:217], v[222:225], v[70:73]
	v_add_u32_e32 v0, s0, v145
	s_waitcnt lgkmcnt(2)
	v_mfma_f32_16x16x32_bf16 v[206:209], v[94:97], v[218:221], v[98:101]
	v_mfma_f32_16x16x32_bf16 v[74:77], v[94:97], v[222:225], v[74:77]
	ds_read_b128 v[94:97], v0
	ds_read_b128 v[214:217], v197 offset:3072
	ds_read_b128 v[228:231], v197 offset:7168
	s_waitcnt lgkmcnt(4)
	v_mfma_f32_16x16x32_bf16 v[210:213], v[202:205], v[218:221], v[210:213]
	v_mfma_f32_16x16x32_bf16 v[86:89], v[202:205], v[222:225], v[86:89]
	ds_read_b128 v[202:205], v0 offset:4096
	ds_read_b128 v[232:235], v0 offset:8192
	s_waitcnt lgkmcnt(5)
	v_mfma_f32_16x16x32_bf16 v[218:221], v[198:201], v[218:221], v[78:81]
	v_mfma_f32_16x16x32_bf16 v[198:201], v[198:201], v[222:225], v[82:85]
	s_waitcnt lgkmcnt(2)
	v_mfma_f32_16x16x32_bf16 v[82:85], v[94:97], v[228:231], v[70:73]
	s_nop 2
	ds_read_b128 v[70:73], v0 offset:12288
	v_mfma_f32_16x16x32_bf16 v[98:101], v[94:97], v[214:217], v[90:93]
	s_waitcnt lgkmcnt(2)
	v_mfma_f32_16x16x32_bf16 v[94:97], v[202:205], v[214:217], v[206:209]
	v_mfma_f32_16x16x32_bf16 v[78:81], v[202:205], v[228:231], v[74:77]
	s_waitcnt lgkmcnt(1)
	v_mfma_f32_16x16x32_bf16 v[90:93], v[232:235], v[214:217], v[210:213]
	v_mfma_f32_16x16x32_bf16 v[74:77], v[232:235], v[228:231], v[86:89]
	s_ashr_i32 s0, s22, 5
	v_lshl_add_u32 v137, s0, 2, v148
	ds_read_b32 v0, v137
	s_waitcnt lgkmcnt(1)
	v_mfma_f32_16x16x32_bf16 v[86:89], v[70:73], v[214:217], v[218:221]
	s_lshl_b32 s82, 1, s22
	v_lshl_or_b32 v2, s22, 6, v149
	v_sub_u32_e32 v4, v160, v2
	v_mfma_f32_16x16x32_bf16 v[70:73], v[70:73], v[228:231], v[198:201]
	s_waitcnt lgkmcnt(0)
	v_and_b32_e32 v0, s82, v0
	v_cmp_ne_u32_e32 vcc, 0, v0
	v_cmp_lt_i32_e64 s[0:1], -1, v4
	s_and_b64 s[22:23], vcc, s[0:1]
	v_mov_b32_e32 v135, 0xff800000
	v_mov_b32_e32 v136, 0xff800000
	s_and_saveexec_b64 s[0:1], s[22:23]
	s_cbranch_execz .LBB0_714
	v_min_u32_e32 v0, 0x7f, v4
	v_lshl_add_u32 v0, v0, 2, v196
	ds_read_b32 v136, v0
	s_waitcnt lgkmcnt(0)
	v_fmac_f32_e32 v136, 0x3fb8aa3b, v98

.LBB0_780:
	v_sub_f32_e32 v0, v89, v72
	v_exp_f32_e32 v0, v0
	v_sub_f32_e32 v73, v88, v72
	v_exp_f32_e32 v73, v73
	v_sub_f32_e32 v83, v83, v72
	v_exp_f32_e32 v125, v83
	v_sub_f32_e32 v82, v82, v72
	v_exp_f32_e32 v134, v82
	v_sub_f32_e32 v83, v85, v72
	v_add_f32_e32 v82, 0, v0
	v_exp_f32_e32 v198, v83
	v_sub_f32_e32 v83, v84, v72
	v_add_f32_e32 v82, v73, v82
	v_exp_f32_e32 v199, v83
	v_sub_f32_e32 v79, v79, v72
	v_add_f32_e32 v82, v125, v82
	v_exp_f32_e32 v200, v79
	v_sub_f32_e32 v78, v78, v72
	v_add_f32_e32 v82, v134, v82
	v_exp_f32_e32 v201, v78
	v_sub_f32_e32 v79, v81, v72
	v_add_f32_e32 v78, v198, v82
	v_exp_f32_e32 v202, v79
	v_sub_f32_e32 v79, v80, v72
	v_add_f32_e32 v78, v199, v78
	v_exp_f32_e32 v203, v79
	v_sub_f32_e32 v75, v75, v72
	v_add_f32_e32 v78, v200, v78
	v_exp_f32_e32 v204, v75
	v_sub_f32_e32 v74, v74, v72
	v_add_f32_e32 v78, v201, v78
	v_exp_f32_e32 v205, v74
	v_sub_f32_e32 v75, v77, v72
	v_add_f32_e32 v74, v202, v78
	v_exp_f32_e32 v206, v75
	v_sub_f32_e32 v75, v76, v72
	v_add_f32_e32 v74, v203, v74
	v_exp_f32_e32 v207, v75
	v_sub_f32_e32 v75, v137, v72
	v_add_f32_e32 v74, v204, v74
	v_exp_f32_e32 v137, v75
	v_sub_f32_e32 v70, v70, v72
	v_add_f32_e32 v74, v205, v74
	v_exp_f32_e32 v208, v70
	v_add_f32_e32 v70, v206, v74
	v_add_f32_e32 v70, v207, v70
	v_add_f32_e32 v70, v137, v70
	v_add_f32_e32 v70, v208, v70
	v_fmac_f32_e32 v70, v5, v4
	v_sub_f32_e32 v4, v136, v71
	v_exp_f32_e32 v5, v4
	v_sub_f32_e32 v4, v135, v71
	v_exp_f32_e32 v82, v4
	v_sub_f32_e32 v4, v99, v71
	v_exp_f32_e32 v83, v4
	v_sub_f32_e32 v4, v98, v71
	v_exp_f32_e32 v84, v4
	v_sub_f32_e32 v74, v101, v71
	v_add_f32_e32 v4, 0, v5
	v_exp_f32_e32 v85, v74
	v_sub_f32_e32 v74, v100, v71
	v_add_f32_e32 v4, v82, v4
	v_exp_f32_e32 v88, v74
	v_sub_f32_e32 v74, v95, v71
	v_add_f32_e32 v4, v83, v4
	v_exp_f32_e32 v89, v74
	v_sub_f32_e32 v74, v94, v71
	v_add_f32_e32 v4, v84, v4
	v_exp_f32_e32 v94, v74
	v_sub_f32_e32 v74, v97, v71
	v_add_f32_e32 v4, v85, v4
	v_exp_f32_e32 v95, v74
	v_sub_f32_e32 v74, v96, v71
	v_add_f32_e32 v4, v88, v4
	v_exp_f32_e32 v96, v74
	v_sub_f32_e32 v74, v91, v71
	v_add_f32_e32 v4, v89, v4
	v_exp_f32_e32 v97, v74
	v_sub_f32_e32 v74, v90, v71
	v_add_f32_e32 v4, v94, v4
	v_exp_f32_e32 v98, v74
	v_sub_f32_e32 v74, v93, v71
	v_add_f32_e32 v4, v95, v4
	v_exp_f32_e32 v99, v74
	v_sub_f32_e32 v74, v92, v71
	v_add_f32_e32 v4, v96, v4
	v_exp_f32_e32 v100, v74
	v_sub_f32_e32 v74, v87, v71
	v_add_f32_e32 v4, v97, v4
	v_exp_f32_e32 v101, v74
	v_sub_f32_e32 v74, v86, v71
	v_add_f32_e32 v4, v98, v4
	v_exp_f32_e32 v135, v74
	v_add_f32_e32 v4, v99, v4
	v_add_f32_e32 v4, v100, v4
	s_cmp_eq_u32 s83, 0
	v_add_f32_e32 v4, v101, v4
	s_cselect_b32 s0, 0x8000, s79
	v_add_f32_e32 v4, v135, v4
	s_add_i32 s0, s0, 0
	v_fmac_f32_e32 v4, v133, v2
	v_add_u32_e32 v2, s0, v142
	ds_read_b128 v[74:77], v2
	ds_read_b128 v[78:81], v2 offset:2048
	v_cvt_pk_bf16_f32 v83, v83, v84
	v_cvt_pk_bf16_f32 v84, v85, v88
	v_cvt_pk_bf16_f32 v85, v89, v94
	ds_read_b128 v[86:89], v2 offset:4096
	v_cvt_pk_bf16_f32 v82, v5, v82
	v_cvt_pk_bf16_f32 v90, v0, v73
	v_cvt_pk_bf16_f32 v91, v125, v134
	v_cvt_pk_bf16_f32 v92, v198, v199
	v_cvt_pk_bf16_f32 v93, v200, v201
	s_waitcnt lgkmcnt(2)
	v_mfma_f32_16x16x32_bf16 v[66:69], v[74:77], v[82:85], v[66:69]
	v_mfma_f32_16x16x32_bf16 v[34:37], v[74:77], v[90:93], v[34:37]
	ds_read_b128 v[74:77], v2 offset:6144
	s_waitcnt lgkmcnt(2)
	v_mfma_f32_16x16x32_bf16 v[62:65], v[78:81], v[82:85], v[62:65]
	v_mfma_f32_16x16x32_bf16 v[30:33], v[78:81], v[90:93], v[30:33]
	ds_read_b128 v[78:81], v2 offset:8192
	s_waitcnt lgkmcnt(2)
	v_mfma_f32_16x16x32_bf16 v[58:61], v[86:89], v[82:85], v[58:61]
	v_mfma_f32_16x16x32_bf16 v[26:29], v[86:89], v[90:93], v[26:29]
	ds_read_b128 v[86:89], v2 offset:10240
	s_waitcnt lgkmcnt(2)
	v_mfma_f32_16x16x32_bf16 v[54:57], v[74:77], v[82:85], v[54:57]
	v_mfma_f32_16x16x32_bf16 v[22:25], v[74:77], v[90:93], v[22:25]
	ds_read_b128 v[74:77], v2 offset:12288
	s_waitcnt lgkmcnt(2)
	v_mfma_f32_16x16x32_bf16 v[50:53], v[78:81], v[82:85], v[50:53]
	v_mfma_f32_16x16x32_bf16 v[18:21], v[78:81], v[90:93], v[18:21]
	ds_read_b128 v[78:81], v2 offset:14336
	v_add_u32_e32 v0, s0, v146
	s_waitcnt lgkmcnt(2)
	v_mfma_f32_16x16x32_bf16 v[46:49], v[86:89], v[82:85], v[46:49]
	v_mfma_f32_16x16x32_bf16 v[14:17], v[86:89], v[90:93], v[14:17]
	ds_read_b128 v[86:89], v0
	s_waitcnt lgkmcnt(2)
	v_mfma_f32_16x16x32_bf16 v[42:45], v[74:77], v[82:85], v[42:45]
	v_mfma_f32_16x16x32_bf16 v[10:13], v[74:77], v[90:93], v[10:13]
	ds_read_b128 v[74:77], v0 offset:2048
	s_waitcnt lgkmcnt(2)
	v_mfma_f32_16x16x32_bf16 v[38:41], v[78:81], v[82:85], v[38:41]
	v_cvt_pk_bf16_f32 v82, v202, v203
	v_cvt_pk_bf16_f32 v83, v204, v205
	v_cvt_pk_bf16_f32 v84, v206, v207
	v_mfma_f32_16x16x32_bf16 v[6:9], v[78:81], v[90:93], v[6:9]
	ds_read_b128 v[90:93], v0 offset:4096
	v_cvt_pk_bf16_f32 v78, v95, v96
	v_cvt_pk_bf16_f32 v79, v97, v98
	v_cvt_pk_bf16_f32 v80, v99, v100
	v_cvt_pk_bf16_f32 v81, v101, v135
	v_cvt_pk_bf16_f32 v85, v137, v208
	s_nop 0
	s_waitcnt lgkmcnt(2)
	v_mfma_f32_16x16x32_bf16 v[66:69], v[86:89], v[78:81], v[66:69]
	v_mfma_f32_16x16x32_bf16 v[34:37], v[86:89], v[82:85], v[34:37]
	ds_read_b128 v[86:89], v0 offset:6144
	s_waitcnt lgkmcnt(2)
	v_mfma_f32_16x16x32_bf16 v[62:65], v[74:77], v[78:81], v[62:65]
	v_mfma_f32_16x16x32_bf16 v[30:33], v[74:77], v[82:85], v[30:33]
	ds_read_b128 v[74:77], v0 offset:8192
	s_waitcnt lgkmcnt(2)
	v_mfma_f32_16x16x32_bf16 v[58:61], v[90:93], v[78:81], v[58:61]
	v_mfma_f32_16x16x32_bf16 v[26:29], v[90:93], v[82:85], v[26:29]
	ds_read_b128 v[90:93], v0 offset:10240
	s_waitcnt lgkmcnt(2)
	v_mfma_f32_16x16x32_bf16 v[54:57], v[86:89], v[78:81], v[54:57]
	v_mfma_f32_16x16x32_bf16 v[22:25], v[86:89], v[82:85], v[22:25]
	ds_read_b128 v[86:89], v0 offset:12288
	s_waitcnt lgkmcnt(2)
	v_mfma_f32_16x16x32_bf16 v[50:53], v[74:77], v[78:81], v[50:53]
	v_mfma_f32_16x16x32_bf16 v[18:21], v[74:77], v[82:85], v[18:21]
	ds_read_b128 v[74:77], v0 offset:14336
	s_waitcnt lgkmcnt(2)
	v_mfma_f32_16x16x32_bf16 v[46:49], v[90:93], v[78:81], v[46:49]
	v_mfma_f32_16x16x32_bf16 v[14:17], v[90:93], v[82:85], v[14:17]
	s_waitcnt lgkmcnt(1)
	v_mfma_f32_16x16x32_bf16 v[42:45], v[86:89], v[78:81], v[42:45]
	v_mfma_f32_16x16x32_bf16 v[10:13], v[86:89], v[82:85], v[10:13]
	s_waitcnt lgkmcnt(0)
	v_mfma_f32_16x16x32_bf16 v[38:41], v[74:77], v[78:81], v[38:41]
	s_waitcnt vmcnt(0)
	s_andn2_b64 vcc, exec, s[2:3]
	s_waitcnt vmcnt(0)
	v_mfma_f32_16x16x32_bf16 v[6:9], v[74:77], v[82:85], v[6:9]
	s_cbranch_vccz .Lx702_exit
	s_mov_b32 s32, 0
	v_mov_b32_e32 v5, v70
	v_mov_b32_e32 v133, v4
	v_mov_b32_e32 v125, v71
	v_mov_b32_e32 v134, v72
	s_mov_b32 s82, s33
	s_cmp_ge_i32 s82, s42
	s_mov_b64 s[0:1], -1
	s_cbranch_scc0 .Lx702_704

.Lx702_711:
	s_lshl_b32 s30, s23, 13
	s_ashr_i32 s31, s30, 31
	s_lshl_b32 s0, s23, 6
	s_lshl_b64 s[30:31], s[30:31], 1
	s_add_u32 s30, s46, s30
	s_addc_u32 s31, s47, s31
	s_cmp_eq_u32 s83, 0
	s_cselect_b32 s1, 0x4000, 0
	s_cselect_b32 s23, s79, 0x8000
	s_add_i32 s1, s28, s1
	v_lshl_add_u64 v[240:241], s[30:31], 0, v[102:103]
	s_mov_b32 s100, s1
	s_ashr_i32 s1, s0, 31
	s_lshl_b64 s[0:1], s[0:1], 1
	s_add_u32 s0, s44, s0
	v_lshl_add_u64 v[242:243], s[30:31], 0, v[108:109]
	s_addc_u32 s1, s45, s1
	s_add_i32 s23, s28, s23
	v_lshl_add_u64 v[244:245], s[0:1], 0, v[106:107]
	s_mov_b32 s101, s23
	v_lshl_add_u64 v[246:247], s[0:1], 0, v[112:113]
	s_mov_b32 s32, 1
.Lx702_pd:
	s_lshl_b32 s0, s83, 14
	s_add_i32 s0, s0, 0
	v_add_u32_e32 v0, s0, v140
	s_barrier
	ds_read_b128 v[70:73], v0
	ds_read_b128 v[74:77], v0 offset:4096
	ds_read_b128 v[78:81], v197
	ds_read_b128 v[82:85], v197 offset:4096
	ds_read_b128 v[86:89], v0 offset:8192
	ds_read_b128 v[94:97], v0 offset:12288
	s_cmp_eq_u32 s32, 0
	s_cbranch_scc1 .Lx702_body
	s_mov_b32 m0, s100
	s_nop 0
	global_load_lds_dwordx4 v[240:241], off
	s_add_i32 m0, s100, 0x400
	s_nop 0
	global_load_lds_dwordx4 v[242:243], off
	s_mov_b32 m0, s101
	s_nop 0
	global_load_lds_dwordx4 v[244:245], off
	s_add_i32 m0, s101, 0x400
	s_nop 0
	global_load_lds_dwordx4 v[246:247], off
	s_branch .Lx702_body
.Lx702_exit:
	s_barrier
	s_branch .LBB0_782
	s_nop 0
	s_nop 0
	s_nop 0
	s_nop 0

.LBB0_808:
	s_sub_i32 s0, s33, s42
	s_sub_i32 s47, s0, s43
	s_add_i32 s23, s37, -1
	s_sub_i32 s81, 0, s42
	s_add_i32 s82, s23, 1
	s_cmp_lt_i32 s82, s42
	s_mov_b64 s[0:1], -1
	s_cbranch_scc1 .LBB0_815
	s_branch .LBB0_810
	s_nop 0
	s_nop 0
	s_nop 0
	s_nop 0
	s_nop 0
	s_nop 0
	s_nop 0
	s_nop 0
	s_nop 0
	s_nop 0
	s_nop 0
	s_nop 0
	s_nop 0
	s_nop 0
	s_nop 0
	s_nop 0
	s_nop 0
.LBB0_810:
	s_add_i32 s0, s81, s23
	s_add_i32 s0, s0, 1
	s_cmp_lt_i32 s0, s43
	s_mov_b64 s[0:1], -1
	s_cbranch_scc1 .LBB0_812
	s_add_i32 s0, s47, s23
	s_add_i32 s22, s0, 2
	s_mov_b64 s[0:1], 0

.Lx809_body:
	s_waitcnt lgkmcnt(0)
	v_mfma_f32_16x16x32_bf16 v[90:93], v[70:73], v[78:81], 0
	v_mfma_f32_16x16x32_bf16 v[70:73], v[70:73], v[82:85], 0
	v_add_u32_e32 v0, s2, v143
	ds_read_b128 v[198:201], v0
	ds_read_b128 v[202:205], v197 offset:1024
	ds_read_b128 v[206:209], v197 offset:5120
	v_mfma_f32_16x16x32_bf16 v[98:101], v[74:77], v[78:81], 0
	v_mfma_f32_16x16x32_bf16 v[74:77], v[74:77], v[82:85], 0
	v_mfma_f32_16x16x32_bf16 v[210:213], v[86:89], v[78:81], 0
	ds_read_b128 v[214:217], v0 offset:4096
	v_mfma_f32_16x16x32_bf16 v[86:89], v[86:89], v[82:85], 0
	v_mfma_f32_16x16x32_bf16 v[78:81], v[94:97], v[78:81], 0
	v_mfma_f32_16x16x32_bf16 v[82:85], v[94:97], v[82:85], 0
	ds_read_b128 v[94:97], v0 offset:8192
	s_waitcnt lgkmcnt(3)
	v_mfma_f32_16x16x32_bf16 v[90:93], v[198:201], v[202:205], v[90:93]
	s_waitcnt lgkmcnt(2)
	v_mfma_f32_16x16x32_bf16 v[70:73], v[198:201], v[206:209], v[70:73]
	ds_read_b128 v[198:201], v0 offset:12288
	v_add_u32_e32 v0, s2, v144
	s_waitcnt lgkmcnt(2)
	v_mfma_f32_16x16x32_bf16 v[98:101], v[214:217], v[202:205], v[98:101]
	v_mfma_f32_16x16x32_bf16 v[74:77], v[214:217], v[206:209], v[74:77]
	ds_read_b128 v[214:217], v0
	ds_read_b128 v[218:221], v197 offset:2048
	ds_read_b128 v[222:225], v197 offset:6144
	s_waitcnt lgkmcnt(4)
	v_mfma_f32_16x16x32_bf16 v[210:213], v[94:97], v[202:205], v[210:213]
	v_mfma_f32_16x16x32_bf16 v[86:89], v[94:97], v[206:209], v[86:89]
	ds_read_b128 v[94:97], v0 offset:4096
	s_waitcnt lgkmcnt(4)
	v_mfma_f32_16x16x32_bf16 v[78:81], v[198:201], v[202:205], v[78:81]
	ds_read_b128 v[202:205], v0 offset:8192
	v_mfma_f32_16x16x32_bf16 v[82:85], v[198:201], v[206:209], v[82:85]
	s_waitcnt lgkmcnt(3)
	v_mfma_f32_16x16x32_bf16 v[90:93], v[214:217], v[218:221], v[90:93]
	ds_read_b128 v[198:201], v0 offset:12288
	s_waitcnt lgkmcnt(3)
	v_mfma_f32_16x16x32_bf16 v[70:73], v[214:217], v[222:225], v[70:73]
	v_add_u32_e32 v0, s2, v145
	s_waitcnt lgkmcnt(2)
	v_mfma_f32_16x16x32_bf16 v[206:209], v[94:97], v[218:221], v[98:101]
	v_mfma_f32_16x16x32_bf16 v[74:77], v[94:97], v[222:225], v[74:77]
	ds_read_b128 v[94:97], v0
	ds_read_b128 v[214:217], v197 offset:3072
	ds_read_b128 v[228:231], v197 offset:7168
	s_waitcnt lgkmcnt(4)
	v_mfma_f32_16x16x32_bf16 v[210:213], v[202:205], v[218:221], v[210:213]
	v_mfma_f32_16x16x32_bf16 v[86:89], v[202:205], v[222:225], v[86:89]
	ds_read_b128 v[202:205], v0 offset:4096
	ds_read_b128 v[232:235], v0 offset:8192
	s_waitcnt lgkmcnt(5)
	v_mfma_f32_16x16x32_bf16 v[218:221], v[198:201], v[218:221], v[78:81]
	v_mfma_f32_16x16x32_bf16 v[198:201], v[198:201], v[222:225], v[82:85]
	s_waitcnt lgkmcnt(2)
	v_mfma_f32_16x16x32_bf16 v[82:85], v[94:97], v[228:231], v[70:73]
	s_nop 2
	ds_read_b128 v[70:73], v0 offset:12288
	v_mfma_f32_16x16x32_bf16 v[98:101], v[94:97], v[214:217], v[90:93]
	s_waitcnt lgkmcnt(2)
	v_mfma_f32_16x16x32_bf16 v[94:97], v[202:205], v[214:217], v[206:209]
	v_mfma_f32_16x16x32_bf16 v[78:81], v[202:205], v[228:231], v[74:77]
	s_waitcnt lgkmcnt(1)
	v_mfma_f32_16x16x32_bf16 v[90:93], v[232:235], v[214:217], v[210:213]
	v_mfma_f32_16x16x32_bf16 v[74:77], v[232:235], v[228:231], v[86:89]
	s_waitcnt lgkmcnt(0)
	v_mfma_f32_16x16x32_bf16 v[86:89], v[70:73], v[214:217], v[218:221]
	s_lshl_b32 s33, s22, 6
	v_subrev_u32_e32 v2, s33, v189
	v_cmp_gt_u32_e32 vcc, s80, v2
	v_mfma_f32_16x16x32_bf16 v[70:73], v[70:73], v[228:231], v[198:201]
	v_mov_b32_e32 v135, 0xff800000
	v_mov_b32_e32 v136, 0xff800000
	s_and_saveexec_b64 s[2:3], vcc
	s_cbranch_execz .LBB0_829
	v_min_u32_e32 v0, 0x7f, v2
	v_lshl_add_u32 v0, v0, 2, v196
	ds_read_b32 v136, v0
	s_waitcnt lgkmcnt(0)
	v_fmac_f32_e32 v136, 0x3fb8aa3b, v98

.LBB0_895:
	v_sub_f32_e32 v0, v89, v72
	v_exp_f32_e32 v0, v0
	v_sub_f32_e32 v73, v88, v72
	v_exp_f32_e32 v73, v73
	v_sub_f32_e32 v83, v83, v72
	v_exp_f32_e32 v133, v83
	v_sub_f32_e32 v82, v82, v72
	v_exp_f32_e32 v134, v82
	v_sub_f32_e32 v83, v85, v72
	v_add_f32_e32 v82, 0, v0
	v_exp_f32_e32 v198, v83
	v_sub_f32_e32 v83, v84, v72
	v_add_f32_e32 v82, v73, v82
	v_exp_f32_e32 v199, v83
	v_sub_f32_e32 v79, v79, v72
	v_add_f32_e32 v82, v133, v82
	v_exp_f32_e32 v200, v79
	v_sub_f32_e32 v78, v78, v72
	v_add_f32_e32 v82, v134, v82
	v_exp_f32_e32 v201, v78
	v_sub_f32_e32 v79, v81, v72
	v_add_f32_e32 v78, v198, v82
	v_exp_f32_e32 v202, v79
	v_sub_f32_e32 v79, v80, v72
	v_add_f32_e32 v78, v199, v78
	v_exp_f32_e32 v203, v79
	v_sub_f32_e32 v75, v75, v72
	v_add_f32_e32 v78, v200, v78
	v_exp_f32_e32 v204, v75
	v_sub_f32_e32 v74, v74, v72
	v_add_f32_e32 v78, v201, v78
	v_exp_f32_e32 v205, v74
	v_sub_f32_e32 v75, v77, v72
	v_add_f32_e32 v74, v202, v78
	v_exp_f32_e32 v206, v75
	v_sub_f32_e32 v75, v76, v72
	v_add_f32_e32 v74, v203, v74
	v_exp_f32_e32 v207, v75
	v_sub_f32_e32 v75, v137, v72
	v_add_f32_e32 v74, v204, v74
	v_exp_f32_e32 v137, v75
	v_sub_f32_e32 v70, v70, v72
	v_add_f32_e32 v74, v205, v74
	v_exp_f32_e32 v208, v70
	v_add_f32_e32 v70, v206, v74
	v_add_f32_e32 v70, v207, v70
	v_add_f32_e32 v70, v137, v70
	v_add_f32_e32 v70, v208, v70
	v_fmac_f32_e32 v70, v5, v4
	v_sub_f32_e32 v4, v136, v71
	v_exp_f32_e32 v5, v4
	v_sub_f32_e32 v4, v135, v71
	v_exp_f32_e32 v82, v4
	v_sub_f32_e32 v4, v99, v71
	v_exp_f32_e32 v83, v4
	v_sub_f32_e32 v4, v98, v71
	v_exp_f32_e32 v84, v4
	v_sub_f32_e32 v74, v101, v71
	v_add_f32_e32 v4, 0, v5
	v_exp_f32_e32 v85, v74
	v_sub_f32_e32 v74, v100, v71
	v_add_f32_e32 v4, v82, v4
	v_exp_f32_e32 v88, v74
	v_sub_f32_e32 v74, v95, v71
	v_add_f32_e32 v4, v83, v4
	v_exp_f32_e32 v89, v74
	v_sub_f32_e32 v74, v94, v71
	v_add_f32_e32 v4, v84, v4
	v_exp_f32_e32 v94, v74
	v_sub_f32_e32 v74, v97, v71
	v_add_f32_e32 v4, v85, v4
	v_exp_f32_e32 v95, v74
	v_sub_f32_e32 v74, v96, v71
	v_add_f32_e32 v4, v88, v4
	v_exp_f32_e32 v96, v74
	v_sub_f32_e32 v74, v91, v71
	v_add_f32_e32 v4, v89, v4
	v_exp_f32_e32 v97, v74
	v_sub_f32_e32 v74, v90, v71
	v_add_f32_e32 v4, v94, v4
	v_exp_f32_e32 v98, v74
	v_sub_f32_e32 v74, v93, v71
	v_add_f32_e32 v4, v95, v4
	v_exp_f32_e32 v99, v74
	v_sub_f32_e32 v74, v92, v71
	v_add_f32_e32 v4, v96, v4
	v_exp_f32_e32 v100, v74
	v_sub_f32_e32 v74, v87, v71
	v_add_f32_e32 v4, v97, v4
	v_exp_f32_e32 v101, v74
	v_sub_f32_e32 v74, v86, v71
	v_add_f32_e32 v4, v98, v4
	v_exp_f32_e32 v135, v74
	v_add_f32_e32 v4, v99, v4
	v_add_f32_e32 v4, v100, v4
	s_cmp_eq_u32 s83, 0
	v_add_f32_e32 v4, v101, v4
	s_cselect_b32 s2, 0x8000, s79
	v_add_f32_e32 v4, v135, v4
	s_add_i32 s2, s2, 0
	v_fmac_f32_e32 v4, v125, v2
	v_add_u32_e32 v2, s2, v142
	ds_read_b128 v[74:77], v2
	ds_read_b128 v[78:81], v2 offset:2048
	v_cvt_pk_bf16_f32 v83, v83, v84
	v_cvt_pk_bf16_f32 v84, v85, v88
	v_cvt_pk_bf16_f32 v85, v89, v94
	ds_read_b128 v[86:89], v2 offset:4096
	v_cvt_pk_bf16_f32 v82, v5, v82
	v_cvt_pk_bf16_f32 v90, v0, v73
	v_cvt_pk_bf16_f32 v91, v133, v134
	v_cvt_pk_bf16_f32 v92, v198, v199
	v_cvt_pk_bf16_f32 v93, v200, v201
	s_waitcnt lgkmcnt(2)
	v_mfma_f32_16x16x32_bf16 v[66:69], v[74:77], v[82:85], v[66:69]
	v_mfma_f32_16x16x32_bf16 v[34:37], v[74:77], v[90:93], v[34:37]
	ds_read_b128 v[74:77], v2 offset:6144
	s_waitcnt lgkmcnt(2)
	v_mfma_f32_16x16x32_bf16 v[62:65], v[78:81], v[82:85], v[62:65]
	v_mfma_f32_16x16x32_bf16 v[30:33], v[78:81], v[90:93], v[30:33]
	ds_read_b128 v[78:81], v2 offset:8192
	s_waitcnt lgkmcnt(2)
	v_mfma_f32_16x16x32_bf16 v[58:61], v[86:89], v[82:85], v[58:61]
	v_mfma_f32_16x16x32_bf16 v[26:29], v[86:89], v[90:93], v[26:29]
	ds_read_b128 v[86:89], v2 offset:10240
	s_waitcnt lgkmcnt(2)
	v_mfma_f32_16x16x32_bf16 v[54:57], v[74:77], v[82:85], v[54:57]
	v_mfma_f32_16x16x32_bf16 v[22:25], v[74:77], v[90:93], v[22:25]
	ds_read_b128 v[74:77], v2 offset:12288
	s_waitcnt lgkmcnt(2)
	v_mfma_f32_16x16x32_bf16 v[50:53], v[78:81], v[82:85], v[50:53]
	v_mfma_f32_16x16x32_bf16 v[18:21], v[78:81], v[90:93], v[18:21]
	ds_read_b128 v[78:81], v2 offset:14336
	v_add_u32_e32 v0, s2, v146
	s_waitcnt lgkmcnt(2)
	v_mfma_f32_16x16x32_bf16 v[46:49], v[86:89], v[82:85], v[46:49]
	v_mfma_f32_16x16x32_bf16 v[14:17], v[86:89], v[90:93], v[14:17]
	ds_read_b128 v[86:89], v0
	s_waitcnt lgkmcnt(2)
	v_mfma_f32_16x16x32_bf16 v[42:45], v[74:77], v[82:85], v[42:45]
	v_mfma_f32_16x16x32_bf16 v[10:13], v[74:77], v[90:93], v[10:13]
	ds_read_b128 v[74:77], v0 offset:2048
	s_waitcnt lgkmcnt(2)
	v_mfma_f32_16x16x32_bf16 v[38:41], v[78:81], v[82:85], v[38:41]
	v_cvt_pk_bf16_f32 v82, v202, v203
	v_cvt_pk_bf16_f32 v83, v204, v205
	v_cvt_pk_bf16_f32 v84, v206, v207
	v_mfma_f32_16x16x32_bf16 v[6:9], v[78:81], v[90:93], v[6:9]
	ds_read_b128 v[90:93], v0 offset:4096
	v_cvt_pk_bf16_f32 v78, v95, v96
	v_cvt_pk_bf16_f32 v79, v97, v98
	v_cvt_pk_bf16_f32 v80, v99, v100
	v_cvt_pk_bf16_f32 v81, v101, v135
	v_cvt_pk_bf16_f32 v85, v137, v208
	s_nop 0
	s_waitcnt lgkmcnt(2)
	v_mfma_f32_16x16x32_bf16 v[66:69], v[86:89], v[78:81], v[66:69]
	v_mfma_f32_16x16x32_bf16 v[34:37], v[86:89], v[82:85], v[34:37]
	ds_read_b128 v[86:89], v0 offset:6144
	s_waitcnt lgkmcnt(2)
	v_mfma_f32_16x16x32_bf16 v[62:65], v[74:77], v[78:81], v[62:65]
	v_mfma_f32_16x16x32_bf16 v[30:33], v[74:77], v[82:85], v[30:33]
	ds_read_b128 v[74:77], v0 offset:8192
	s_waitcnt lgkmcnt(2)
	v_mfma_f32_16x16x32_bf16 v[58:61], v[90:93], v[78:81], v[58:61]
	v_mfma_f32_16x16x32_bf16 v[26:29], v[90:93], v[82:85], v[26:29]
	ds_read_b128 v[90:93], v0 offset:10240
	s_waitcnt lgkmcnt(2)
	v_mfma_f32_16x16x32_bf16 v[54:57], v[86:89], v[78:81], v[54:57]
	v_mfma_f32_16x16x32_bf16 v[22:25], v[86:89], v[82:85], v[22:25]
	ds_read_b128 v[86:89], v0 offset:12288
	s_waitcnt lgkmcnt(2)
	v_mfma_f32_16x16x32_bf16 v[50:53], v[74:77], v[78:81], v[50:53]
	v_mfma_f32_16x16x32_bf16 v[18:21], v[74:77], v[82:85], v[18:21]
	ds_read_b128 v[74:77], v0 offset:14336
	s_waitcnt lgkmcnt(2)
	v_mfma_f32_16x16x32_bf16 v[46:49], v[90:93], v[78:81], v[46:49]
	v_mfma_f32_16x16x32_bf16 v[14:17], v[90:93], v[82:85], v[14:17]
	s_waitcnt lgkmcnt(1)
	v_mfma_f32_16x16x32_bf16 v[42:45], v[86:89], v[78:81], v[42:45]
	v_mfma_f32_16x16x32_bf16 v[10:13], v[86:89], v[82:85], v[10:13]
	s_waitcnt lgkmcnt(0)
	v_mfma_f32_16x16x32_bf16 v[38:41], v[74:77], v[78:81], v[38:41]
	s_waitcnt vmcnt(0)
	s_andn2_b64 vcc, exec, s[0:1]
	s_waitcnt vmcnt(0)
	v_mfma_f32_16x16x32_bf16 v[6:9], v[74:77], v[82:85], v[6:9]
	s_cbranch_vccz .Lx809_exit
	s_mov_b32 s32, 0
	s_mov_b32 s23, s82
	v_mov_b32_e32 v5, v70
	v_mov_b32_e32 v125, v4
	v_mov_b32_e32 v133, v71
	v_mov_b32_e32 v134, v72
	s_add_i32 s82, s23, 1
	s_cmp_lt_i32 s82, s42
	s_mov_b64 s[0:1], -1
	s_cbranch_scc1 .Lx809_815

.Lx809_826:
	s_lshl_b32 s2, s30, 6
	s_lshl_b32 s30, s30, 13
	s_ashr_i32 s31, s30, 31
	s_lshl_b64 s[30:31], s[30:31], 1
	s_add_u32 s30, s8, s30
	s_addc_u32 s31, s44, s31
	s_cmp_eq_u32 s83, 0
	s_cselect_b32 s3, 0x4000, 0
	s_cselect_b32 s23, s79, 0x8000
	s_add_i32 s3, s28, s3
	v_lshl_add_u64 v[240:241], s[30:31], 0, v[102:103]
	s_mov_b32 s100, s3
	s_ashr_i32 s3, s2, 31
	s_lshl_b64 s[2:3], s[2:3], 1
	s_add_u32 s2, s45, s2
	v_lshl_add_u64 v[242:243], s[30:31], 0, v[108:109]
	s_addc_u32 s3, s46, s3
	s_add_i32 s23, s28, s23
	v_lshl_add_u64 v[244:245], s[2:3], 0, v[106:107]
	s_mov_b32 s101, s23
	v_lshl_add_u64 v[246:247], s[2:3], 0, v[112:113]
	s_mov_b32 s32, 1
.Lx809_pd:
	s_lshl_b32 s2, s83, 14
	s_add_i32 s2, s2, 0
	v_add_u32_e32 v0, s2, v140
	s_barrier
	ds_read_b128 v[70:73], v0
	ds_read_b128 v[74:77], v0 offset:4096
	ds_read_b128 v[78:81], v197
	ds_read_b128 v[82:85], v197 offset:4096
	ds_read_b128 v[86:89], v0 offset:8192
	ds_read_b128 v[94:97], v0 offset:12288
	s_cmp_eq_u32 s32, 0
	s_cbranch_scc1 .Lx809_body
	s_mov_b32 m0, s100
	s_nop 0
	global_load_lds_dwordx4 v[240:241], off
	s_add_i32 m0, s100, 0x400
	s_nop 0
	global_load_lds_dwordx4 v[242:243], off
	s_mov_b32 m0, s101
	s_nop 0
	global_load_lds_dwordx4 v[244:245], off
	s_add_i32 m0, s101, 0x400
	s_nop 0
	global_load_lds_dwordx4 v[246:247], off
	s_branch .Lx809_body
.Lx809_exit:
	s_barrier
	s_branch .LBB0_518

.LBB0_902:
	s_or_b64 exec, exec, s[0:1]
	v_and_b32_e32 v0, 15, v38
	v_bitop3_b32 v40, v1, v0, 3 bitop3:0x6c
	v_bitop3_b32 v47, v1, v38, 3 bitop3:0x6c
	v_and_b32_e32 v51, 0x7f, v38
	v_lshlrev_b32_e32 v46, 4, v40
	v_lshlrev_b32_e32 v40, 7, v0
	v_lshlrev_b32_e32 v41, 3, v47
	s_movk_i32 s1, 0x70
	v_lshlrev_b32_e32 v142, 2, v51
	v_and_or_b32 v48, v41, s1, v40
	v_lshlrev_b32_e32 v40, 3, v1
	v_lshl_or_b32 v82, s6, 9, v142
	v_and_b32_e32 v49, 8, v40
	v_lshl_add_u64 v[40:41], s[74:75], 0, v[82:83]
	s_movk_i32 s6, 0x7000
	v_add_co_u32_e32 v42, vcc, s6, v40
	s_movk_i32 s6, 0x6000
	s_nop 0
	v_addc_co_u32_e32 v43, vcc, 0, v41, vcc
	global_load_dword v197, v82, s[76:77]
	global_load_dword v193, v[42:43], off offset:2048
	global_load_dword v194, v[42:43], off
	v_add_co_u32_e32 v42, vcc, s6, v40
	s_movk_i32 s6, 0x5000
	s_nop 0
	v_addc_co_u32_e32 v43, vcc, 0, v41, vcc
	global_load_dword v195, v[42:43], off offset:2048
	global_load_dword v196, v[42:43], off
	v_add_co_u32_e32 v42, vcc, s6, v40
	s_movk_i32 s6, 0x4000
	s_nop 0
	v_addc_co_u32_e32 v43, vcc, 0, v41, vcc
	global_load_dword v198, v[42:43], off offset:2048
	global_load_dword v199, v[42:43], off
	v_add_co_u32_e32 v42, vcc, s6, v40
	s_movk_i32 s43, 0x3000
	s_nop 0
	v_addc_co_u32_e32 v43, vcc, 0, v41, vcc
	global_load_dword v200, v[42:43], off offset:2048
	global_load_dword v201, v[42:43], off
	v_add_co_u32_e32 v42, vcc, s43, v40
	s_movk_i32 s6, 0x2000
	s_nop 0
	v_addc_co_u32_e32 v43, vcc, 0, v41, vcc
	global_load_dword v202, v[42:43], off offset:2048
	global_load_dword v203, v[42:43], off
	v_add_co_u32_e32 v42, vcc, s6, v40
	s_movk_i32 s6, 0x1000
	s_nop 0
	v_addc_co_u32_e32 v43, vcc, 0, v41, vcc
	v_add_co_u32_e32 v40, vcc, s6, v40
	global_load_dword v204, v[42:43], off offset:2048
	global_load_dword v205, v[42:43], off
	v_addc_co_u32_e32 v41, vcc, 0, v41, vcc
	global_load_dword v206, v[40:41], off offset:2048
	global_load_dword v207, v[40:41], off
	global_load_dword v209, v82, s[74:75] offset:2048
	global_load_dword v208, v82, s[74:75]
	s_ashr_i32 s0, s2, 6
	s_and_b32 s37, s0, 3
	s_ashr_i32 s3, s2, 8
	v_readlane_b32 s70, v252, 2
	v_readlane_b32 s71, v252, 3
	s_add_u32 s38, s70, 0x42490a00
	v_and_b32_e32 v44, 3, v1
	s_addc_u32 s39, s71, 0
	s_add_i32 s16, 0, 0x21800
	v_and_b32_e32 v42, 0xffffff00, v39
	v_and_b32_e32 v52, 0xfffffe00, v39
	v_lshlrev_b32_e32 v39, 5, v38
	s_and_b32 s2, s2, 0xffffff00
	s_add_i32 s6, 0, 0x20000
	v_and_b32_e32 v53, 0xffffffc0, v39
	v_and_b32_e32 v54, 32, v39
	v_lshl_or_b32 v147, v44, 3, s2
	s_add_i32 s2, s16, s2
	s_lshl_b32 s18, s37, 6
	v_lshlrev_b32_e32 v40, 2, v0
	v_add3_u32 v143, s6, v53, v54
	v_lshlrev_b32_e32 v51, 1, v51
	v_lshlrev_b32_e32 v54, 1, v38
	s_add_i32 s2, s2, s18
	s_add_i32 s18, s18, s16
	v_and_b32_e32 v54, 14, v54
	v_add_u32_e32 v148, s2, v40
	v_add_u32_e32 v149, s18, v40
	v_and_b32_e32 v40, 0xfffff000, v39
	v_and_b32_e32 v39, 0xf0, v51
	v_or3_b32 v151, v39, v54, v40
	v_mov_b32_e32 v39, 0x100
	v_bitop3_b32 v152, v151, 16, v39 bitop3:0x36
	v_mov_b32_e32 v39, 0x200
	v_bitop3_b32 v153, v151, 32, v39 bitop3:0x36
	v_mov_b32_e32 v39, 0x300
	v_bitop3_b32 v154, v151, 48, v39 bitop3:0x36
	v_mov_b32_e32 v39, 0x400
	v_bitop3_b32 v155, v151, 64, v39 bitop3:0x36
	s_movk_i32 s2, 0x50
	v_mov_b32_e32 v39, 0x500
	v_bitop3_b32 v156, v151, s2, v39 bitop3:0x36
	s_movk_i32 s66, 0x60
	v_mov_b32_e32 v39, 0x600
	v_bitop3_b32 v157, v151, s66, v39 bitop3:0x36
	v_mov_b32_e32 v39, 0x700
	v_bitop3_b32 v158, v151, s1, v39 bitop3:0x36
	s_movk_i32 s1, 0x80
	v_mov_b32_e32 v39, 0x800
	v_bitop3_b32 v159, v151, s1, v39 bitop3:0x36
	s_movk_i32 s2, 0x90
	v_mov_b32_e32 v39, 0x900
	v_ashrrev_i32_e32 v56, 8, v38
	v_bitop3_b32 v160, v151, s2, v39 bitop3:0x36
	s_movk_i32 s2, 0xa0
	v_mov_b32_e32 v39, 0xa00
	s_mov_b64 s[82:83], s[78:79]
	v_lshl_add_u32 v57, v56, 14, 0
	v_bfe_u32 v59, v38, 1, 3
	v_lshlrev_b32_e32 v56, 2, v56
	s_lshl_b32 s14, s37, 12
	v_bitop3_b32 v161, v151, s2, v39 bitop3:0x36
	s_movk_i32 s2, 0xb0
	v_mov_b32_e32 v39, 0xb00
	s_mov_b64 s[80:81], s[76:77]
	v_bitop3_b32 v60, v56, v140, 7 bitop3:0x78
	v_bitop3_b32 v61, v56, v59, 1 bitop3:0x36
	v_bitop3_b32 v62, v56, v59, 2 bitop3:0x36
	v_bitop3_b32 v56, v56, v59, 3 bitop3:0x36
	s_add_i32 s76, s14, 0
	v_lshlrev_b32_e32 v59, 2, v44
	s_lshl_b32 s14, s3, 15
	v_bitop3_b32 v162, v151, s2, v39 bitop3:0x36
	s_movk_i32 s2, 0xc0
	v_mov_b32_e32 v39, 0xc00
	v_ashrrev_i32_e32 v53, 7, v38
	s_lshl_b32 s17, s0, 3
	s_add_i32 s77, s14, 0
	s_lshl_b32 s14, s3, 14
	v_lshl_or_b32 v150, s3, 7, v59
	v_bitop3_b32 v163, v151, s2, v39 bitop3:0x36
	s_movk_i32 s3, 0xd0
	v_mov_b32_e32 v39, 0xd00
	v_lshl_add_u32 v144, v53, 10, s6
	s_add_i32 s6, 0, 0x21000
	v_bitop3_b32 v164, v151, s3, v39 bitop3:0x36
	s_movk_i32 s3, 0xe0
	v_mov_b32_e32 v39, 0xe00
	s_lshl_b32 s78, s0, 13
	s_or_b32 s0, s17, 1
	v_lshl_add_u32 v145, v38, 2, s6
	v_add_u32_e32 v146, s6, v142
	v_cmp_lt_i32_e64 s[6:7], 0, v53
	s_movk_i32 s44, 0xf0
	v_bitop3_b32 v165, v151, s3, v39 bitop3:0x36
	v_mov_b32_e32 v39, 0xf00
	s_lshl_b32 s3, s0, 2
	s_lshl_b32 s86, s0, 10
	s_or_b32 s0, s17, 2
	v_writelane_b32 v253, s6, 4
	v_bitop3_b32 v166, v151, s44, v39 bitop3:0x36
	v_lshlrev_b32_e32 v39, 4, v47
	v_bitop3_b32 v47, v44, v38, s3 bitop3:0x36
	s_lshl_b32 s3, s0, 2
	s_lshl_b32 s87, s0, 10
	s_or_b32 s0, s17, 5
	v_writelane_b32 v253, s7, 5
	v_cmp_lt_i32_e64 s[6:7], 1, v53
	v_cmp_lt_i32_e64 s[8:9], 2, v53
	v_cmp_lt_i32_e64 s[74:75], 3, v53
	v_add_u32_e32 v53, 0, v51
	v_bitop3_b32 v51, v44, v38, s3 bitop3:0x36
	s_lshl_b32 s3, s0, 2
	s_lshl_b32 s90, s0, 10
	s_or_b32 s0, s17, 6
	v_bitop3_b32 v54, v44, v38, s3 bitop3:0x36
	s_lshl_b32 s3, s0, 2
	v_and_b32_e32 v55, 0xff, v38
	s_add_i32 s72, 0, 0x18000
	v_bitop3_b32 v63, v44, v38, s3 bitop3:0x36
	v_bitop3_b32 v38, v44, v38, 12 bitop3:0x36
	v_lshlrev_b32_e32 v45, 8, v0
	v_lshlrev_b32_e32 v58, 1, v55
	v_lshl_add_u32 v55, v55, 7, s72
	s_add_i32 s76, s76, 0x14000
	s_add_i32 s72, s72, s14
	s_or_b32 s88, s78, 0xc00
	s_or_b32 s89, s78, 0x1000
	s_lshl_b32 s91, s0, 10
	v_lshlrev_b32_e32 v64, 4, v38
	s_or_b32 s92, s78, 0x1c00
	v_or_b32_e32 v38, 2, v59
	v_bitop3_b32 v169, v46, s2, v45 bitop3:0x36
	s_cmp_eq_u32 s37, 0
	v_cmp_gt_u32_e64 s[2:3], v38, v0
	v_or_b32_e32 v38, 3, v59
	v_bitop3_b32 v168, v46, s1, v45 bitop3:0x36
	s_cselect_b64 s[62:63], -1, 0
	v_cmp_gt_u32_e32 vcc, v59, v0
	v_cmp_ge_u32_e64 s[0:1], v59, v0
	v_cmp_gt_u32_e64 s[22:23], v38, v0
	s_and_b64 s[56:57], s[62:63], vcc
	s_and_b64 s[40:41], s[62:63], s[0:1]
	s_and_b64 s[48:49], s[62:63], s[2:3]
	s_and_b64 s[50:51], s[62:63], s[22:23]
	s_cmp_eq_u32 s37, 1
	s_cselect_b64 s[18:19], -1, 0
	s_and_b64 s[20:21], s[18:19], vcc
	s_and_b64 s[46:47], s[18:19], s[0:1]
	s_and_b64 s[60:61], s[18:19], s[2:3]
	s_and_b64 s[64:65], s[18:19], s[22:23]
	s_cmp_gt_u32 s37, 1
	s_cselect_b64 s[52:53], -1, 0
	s_cmp_eq_u32 s37, 2
	v_writelane_b32 v253, s8, 6
	s_cselect_b64 s[58:59], -1, 0
	v_lshlrev_b32_e32 v82, 2, v150
	v_writelane_b32 v253, s9, 7
	s_and_b64 s[8:9], s[58:59], vcc
	v_writelane_b32 v253, s8, 8
	v_or_b32_e32 v170, 16, v150
	v_lshl_add_u64 v[84:85], s[82:83], 0, v[82:83]
	v_writelane_b32 v253, s9, 9
	s_and_b64 s[8:9], s[58:59], s[0:1]
	v_writelane_b32 v253, s8, 10
	v_lshlrev_b32_e32 v82, 2, v170
	v_or_b32_e32 v171, 32, v150
	v_writelane_b32 v253, s9, 11
	s_and_b64 s[8:9], s[58:59], s[2:3]
	v_lshl_add_u64 v[86:87], s[82:83], 0, v[82:83]
	v_lshlrev_b32_e32 v82, 2, v171
	v_or_b32_e32 v172, 48, v150
	v_writelane_b32 v253, s8, 12
	v_lshl_add_u64 v[88:89], s[82:83], 0, v[82:83]
	v_lshlrev_b32_e32 v82, 2, v172
	v_or_b32_e32 v173, 64, v150
	v_writelane_b32 v253, s9, 13
	s_and_b64 s[8:9], s[58:59], s[22:23]
	v_lshl_add_u64 v[90:91], s[82:83], 0, v[82:83]
	v_lshlrev_b32_e32 v82, 2, v173
	v_or_b32_e32 v174, 0x50, v150
	s_cmp_lg_u32 s37, 3
	v_lshl_add_u64 v[92:93], s[82:83], 0, v[82:83]
	v_lshlrev_b32_e32 v82, 2, v174
	v_or_b32_e32 v175, 0x60, v150
	v_writelane_b32 v253, s8, 14
	s_cselect_b64 s[68:69], -1, 0
	v_lshl_add_u64 v[94:95], s[82:83], 0, v[82:83]
	v_lshlrev_b32_e32 v82, 2, v175
	v_or_b32_e32 v176, 0x70, v150
	v_or_b32_e32 v141, v46, v45
	v_or_b32_e32 v50, v48, v49
	v_bitop3_b32 v167, v46, 64, v45 bitop3:0x36
	v_writelane_b32 v253, s9, 15
	v_bitop3_b32 v45, v48, 32, v49 bitop3:0x36
	v_bitop3_b32 v46, v48, 64, v49 bitop3:0x36
	v_bitop3_b32 v48, v48, s66, v49 bitop3:0x36
	v_lshl_add_u64 v[96:97], s[82:83], 0, v[82:83]
	v_lshlrev_b32_e32 v82, 2, v176
	s_or_b64 s[58:59], s[62:63], s[20:21]
	s_or_b64 s[46:47], s[62:63], s[46:47]
	s_or_b64 s[60:61], s[62:63], s[60:61]
	s_or_b64 s[62:63], s[62:63], s[64:65]
	s_or_b64 s[8:9], s[68:69], s[22:23]
	s_or_b64 s[2:3], s[68:69], s[2:3]
	s_or_b64 s[66:67], s[68:69], s[0:1]
	s_or_b64 s[64:65], s[68:69], vcc
	v_lshl_or_b32 v177, s37, 4, v0
	v_lshl_or_b32 v0, v44, 8, s78
	v_readlane_b32 s68, v252, 0
	v_lshlrev_b32_e32 v47, 4, v47
	v_lshlrev_b32_e32 v54, 4, v54
	v_lshl_add_u64 v[98:99], s[82:83], 0, v[82:83]
	v_and_or_b32 v82, v39, s44, v0
	s_mov_b64 s[0:1], 0x50890a00
	v_readlane_b32 s69, v252, 1
	s_mov_b32 s96, s68
	s_ashr_i32 s97, s68, 31
	s_movk_i32 s45, 0x400
	v_and_b32_e32 v47, 0xf0, v47
	v_lshlrev_b32_e32 v51, 4, v51
	v_and_b32_e32 v54, 0xf0, v54
	v_lshlrev_b32_e32 v63, 4, v63
	v_lshl_add_u64 v[100:101], v[82:83], 0, s[0:1]
	s_lshl_b64 s[68:69], s[96:97], 16
	v_or_b32_e32 v82, 0x1000, v82
	s_movk_i32 s37, 0x1400
	s_movk_i32 s73, 0x800
	v_and_b32_e32 v51, 0xf0, v51
	v_and_b32_e32 v63, 0xf0, v63
	s_add_u32 s68, s70, s68
	v_or3_b32 v38, v0, v47, s45
	v_mov_b32_e32 v39, v83
	v_lshl_add_u64 v[108:109], v[82:83], 0, s[0:1]
	v_or3_b32 v82, v0, v54, s37
	s_movk_i32 s37, 0x1800
	v_cmp_eq_u32_e64 s[54:55], 0, v44
	s_addc_u32 s69, s71, s69
	v_readlane_b32 s70, v252, 6
	v_lshl_add_u64 v[102:103], v[38:39], 0, s[0:1]
	v_or3_b32 v38, v0, v51, s73
	v_and_or_b32 v44, v64, s44, v0
	v_lshl_add_u64 v[110:111], v[82:83], 0, s[0:1]
	v_or3_b32 v82, v0, v63, s37
	s_mov_b32 s80, s70
	v_lshl_add_u64 v[104:105], v[38:39], 0, s[0:1]
	v_or_b32_e32 v38, 0xc00, v44
	v_lshl_add_u64 v[112:113], v[82:83], 0, s[0:1]
	v_or_b32_e32 v82, 0x1c00, v44
	v_lshl_add_u64 v[106:107], v[38:39], 0, s[0:1]
	v_lshl_add_u64 v[114:115], v[82:83], 0, s[0:1]
	s_mov_b32 s0, s80
	v_readlane_b32 s71, v252, 7
	v_writelane_b32 v252, s0, 6
	v_add_u32_e32 v41, 0, v132
	v_add_u32_e32 v43, 0, v134
	v_writelane_b32 v252, s1, 7
	s_mov_b32 s0, s96
	v_lshlrev_b32_e32 v60, 4, v60
	v_lshlrev_b32_e32 v61, 4, v61
	v_lshlrev_b32_e32 v62, 4, v62
	v_lshlrev_b32_e32 v56, 4, v56
	v_writelane_b32 v253, s8, 16
	s_ashr_i32 s81, s70, 31
	v_writelane_b32 v252, s0, 0
	s_mov_b32 s42, 0
	v_writelane_b32 v253, s9, 17
	s_lshl_b64 s[70:71], s[80:81], 16
	s_lshl_b32 s79, s80, 6
	s_lshl_b32 s80, s80, 4
	v_add_u32_e32 v178, v41, v42
	v_add_u32_e32 v179, v43, v52
	s_mov_b32 s81, 0xbfb8aa3b
	s_mov_b32 s82, 0x800000
	s_mov_b32 s83, 0x3f317217
	s_mov_b32 s84, 0x7f800000
	v_add_u32_e32 v180, v53, v40
	s_add_i32 s85, 0, 0x10000
	v_add_u32_e32 v181, v57, v58
	v_add_u32_e32 v182, v55, v60
	v_add_u32_e32 v183, v55, v61
	v_add_u32_e32 v184, v55, v62
	v_add_u32_e32 v185, v55, v56
	s_add_i32 s86, s86, 0
	s_add_i32 s87, s87, 0
	s_add_i32 s88, s88, 0
	s_add_i32 s89, s89, 0
	s_add_i32 s90, s90, 0
	s_add_i32 s91, s91, 0
	s_add_i32 s92, s92, 0
	s_add_i32 s93, 0, 0x11000
	s_add_i32 s94, 0, 0x12000
	s_add_i32 s95, 0, 0x13000
	v_add_u32_e32 v186, s72, v50
	v_add_u32_e32 v187, s72, v45
	v_add_u32_e32 v188, s72, v46
	v_add_u32_e32 v189, s72, v48
	v_mov_b32_e32 v190, 0x3727c5ac
	v_mov_b32_e32 v191, 0x260
	v_mov_b32_e32 v192, 0x41b17218
	v_writelane_b32 v252, s1, 1
	s_branch .LBB0_904
	s_nop 0
	s_nop 0
	s_nop 0
	s_nop 0
	s_nop 0
	s_nop 0
	s_nop 0
	s_nop 0
